# P3 prep: gate-input tile LDS write deferred behind the K/Q requests (one exposed round trip fewer per item)
# speedup vs baseline: 1.0006x; 1.0006x over previous
; #define LAS __attribute__((address_space(3)))
; __device__ __forceinline__ int scan_row(int b, int dir, int s) {
;     if (s < 256) { const int tc = dir ? 255 - s : s; return NT + b * 256 + tc; }
;     const int t0 = s - 256; return b * 2048 + (dir ? 2047 - t0 : t0);
; }
; __device__ __forceinline__ unsigned cvtpk_bf16(float lo, float hi) { unsigned r; asm("v_cvt_pk_bf16_f32 %0, %1, %2" : "=v"(r) : "v"(lo), "v"(hi)); return r; }
; __device__ __forceinline__ void prep_item(const Args& a, LAS unsigned char* lds, int tid, int dir, int b, int ch) {
;     unsigned char* ws = a.ws;
;     const bf16* Q = (const bf16*)(ws + RA_Q); const bf16* Kb = (const bf16*)(ws + RA_K); const float* ALR = (const float*)(ws + RA_ALR);
;     v4u* QG = (v4u*)(ws + PQG); bf16* AM = (bf16*)(ws + PAM); bf16* KD = (bf16*)(ws + PKD); float* DEC = (float*)(ws + PDEC);
;     constexpr int TS = 520;
;     LAS float* alr = (LAS float*)lds;
;     LAS bf16* Kt = (LAS bf16*)(lds + 4096);
;     LAS bf16* Qt = (LAS bf16*)(lds + 4096 + 64 * TS * 2);
;     const int col = tid, h = col >> 7, dk = col & 127;
;     const int lane = tid & 63, wave = __builtin_amdgcn_readfirstlane(tid >> 6), l15 = lane & 15, l4 = lane >> 4;
;     const bool lat = ch >= 4;
;     if (tid < 256) { const int i = tid >> 2, r4 = (tid & 3) * 4; const int row = scan_row(b, dir, ch * 64 + i);
;         *(LAS f32x4*)(alr + i * 16 + r4) = *(const f32x4*)(ALR + (size_t)row * 32 + dir * 16 + r4); }
; __device__ __forceinline__ void phase3_prep(const Args& a, LAS unsigned char* lds, int tid, int vcu, int G, int bx) {
;     ...
;             else if (bx >= 104) { if (k < 2) code = -2 - (2 * (bx - 104) + k); }
;             else { if (k == 0) code = 408 + bx; else if (k == 1 && bx < 32) code = -2 - (32 + bx); }
;             if (code == -1) continue;
;             const bool lat = code >= 0; const int item = lat ? code : -2 - code;
;             const int dir = lat ? item >> 8 : item >> 5, b = lat ? (item >> 5) & 7 : (item >> 2) & 7, ch = lat ? 4 + (item & 31) : (item & 3);
;             prep_item(a, lds, tid, dir, b, ch);
.LBB0_350:
	s_sub_i32 s5, -2, s4
	s_cmp_gt_i32 s4, -1
	s_cselect_b64 s[2:3], -1, 0
	s_and_b64 s[2:3], s[2:3], exec
	s_cselect_b32 s6, s4, s5
	s_and_b32 s75, s6, 31
	s_add_i32 s7, s75, 4
	s_and_b32 s18, s5, 3
	s_cmp_gt_i32 s4, -1
	s_cselect_b64 s[2:3], -1, 0
	s_and_b64 s[2:3], s[2:3], exec
	s_cselect_b32 s21, s7, s18
	s_ashr_i32 s18, s6, 5
	s_lshr_b32 s5, s5, 2
	s_cmp_gt_i32 s4, -1
	s_cselect_b64 s[2:3], -1, 0
	s_and_b64 s[2:3], s[2:3], exec
	s_cselect_b32 s5, s18, s5
	s_ashr_i32 s19, s4, 8
	s_cmp_gt_i32 s4, -1
	s_cselect_b64 s[2:3], -1, 0
	s_and_b64 s[6:7], s[2:3], exec
	s_cselect_b32 s20, s19, s18
	s_cmp_lt_i32 s4, 0
	s_cselect_b64 s[18:19], -1, 0
	s_and_b32 s22, s5, 7
	v_readfirstlane_b32 s76, v66
	s_lshl_b32 s23, s21, 6
	s_and_saveexec_b64 s[4:5], s[0:1]
	s_cbranch_execz .LBB0_356
	v_add_u32_e32 v1, s23, v82
	s_movk_i32 s6, 0xff
	v_cmp_lt_i32_e32 vcc, s6, v1
	s_and_saveexec_b64 s[6:7], vcc
	s_xor_b64 s[6:7], exec, s[6:7]
	s_cmp_eq_u32 s20, 0
	v_add_u32_e32 v2, 0xffffff00, v1
	v_sub_u32_e32 v1, 0x8ff, v1
	s_cselect_b64 vcc, -1, 0
	v_cndmask_b32_e32 v1, v1, v2, vcc
	v_lshl_add_u32 v2, s22, 11, v1
	s_andn2_saveexec_b64 s[6:7], s[6:7]
	s_cmp_eq_u32 s20, 0
	v_sub_u32_e32 v2, 0xff, v1
	s_cselect_b64 vcc, -1, 0
	v_cndmask_b32_e32 v1, v2, v1, vcc
	v_lshl_add_u32 v1, s22, 8, v1
	v_add_u32_e32 v2, 0x4000, v1
	s_or_b64 exec, exec, s[6:7]
	v_ashrrev_i32_e32 v3, 31, v2
	v_lshlrev_b64 v[2:3], 7, v[2:3]
	s_lshl_b32 s6, s20, 4
	v_lshl_add_u64 v[2:3], s[10:11], 0, v[2:3]
	s_ashr_i32 s7, s6, 31
	v_lshl_add_u64 v[2:3], s[6:7], 2, v[2:3]
	v_lshl_add_u64 v[2:3], v[2:3], 0, v[68:69]
	global_load_dwordx4 v[240:243], v[2:3], off

; #define LAS __attribute__((address_space(3)))
; __device__ __forceinline__ void prep_item(const Args& a, LAS unsigned char* lds, int tid, int dir, int b, int ch) {
;     ...
;     if (tid < 256) { const int i = tid >> 2, r4 = (tid & 3) * 4; const int row = scan_row(b, dir, ch * 64 + i);
;         *(LAS f32x4*)(alr + i * 16 + r4) = *(const f32x4*)(ALR + (size_t)row * 32 + dir * 16 + r4); }
;     { v4u kr[8], qr[8];
; #pragma unroll
;       for (int q = 0; q < 8; ++q) { const int p = tid + 512 * q, i = p >> 6, c8 = (p & 63) * 8; const int row = scan_row(b, dir, ch * 64 + i);
;           kr[q] = *(const v4u*)(Kb + (size_t)row * 512 + c8); if (lat) qr[q] = *(const v4u*)(Q + (size_t)row * 512 + c8); }
; #pragma unroll
;       for (int q = 0; q < 8; ++q) { const int p = tid + 512 * q, i = p >> 6, c8 = (p & 63) * 8; *(LAS v4u*)(Kt + i * TS + c8) = kr[q]; if (lat) *(LAS v4u*)(Qt + i * TS + c8) = qr[q]; } }
.LBB0_372:
	s_mov_b64 s[2:3], -1
	s_and_b64 vcc, exec, s[18:19]
	s_waitcnt vmcnt(0)
	s_and_saveexec_b64 s[100:101], s[0:1]
	ds_write_b128 v83, v[240:243]
	s_mov_b64 exec, s[100:101]
	ds_write_b128 v92, v[6:9] offset:4096
	s_cbranch_vccz .LBB0_380
	ds_write_b128 v94, v[10:13] offset:4096
	s_cbranch_execz .LBB0_381
